# main: Wv fragment loads hoisted from the scores phase into phase 1 (new regs v184-247)
# baseline (speedup 1.0000x reference)
_Z7na_mainPKDF16_PKhS0_PKfS4_S4_S4_Pf:
	s_lshl_b32 s3, s2, 5
	s_and_b32 s3, s3, 0xe0
	s_ashr_i32 s2, s2, 3
	s_add_i32 s3, s3, s2
	s_ashr_i32 s2, s3, 6
	s_lshl_b32 s3, s3, 5
	s_and_b32 s14, s3, 0x7e0
	v_mov_b32_e32 v1, 0x7c0
	s_load_dwordx8 s[4:11], s[0:1], 0x0
	s_load_dwordx2 s[18:19], s[0:1], 0x20
	v_med3_u32 v1, s14, 32, v1
	v_subrev_u32_e32 v97, 32, v1
	s_ashr_i32 s3, s2, 31
	v_lshlrev_b32_e32 v58, 1, v97
	s_lshl_b64 s[12:13], s[2:3], 12
	v_mov_b32_e32 v59, 0
	v_sub_u32_e32 v60, s14, v97
	v_lshl_add_u64 v[10:11], s[12:13], 0, v[58:59]
	v_lshlrev_b64 v[2:3], 9, v[10:11]
	v_lshl_or_b32 v22, v60, 6, v0
	s_waitcnt lgkmcnt(0)
	v_and_b32_e32 v208, 31, v0
	v_lshlrev_b32_e32 v208, 5, v208
	global_load_dwordx4 v[192:195], v208, s[18:19]
	global_load_dwordx4 v[196:199], v208, s[18:19] offset:16
	v_lshl_add_u64 v[20:21], s[4:5], 0, v[2:3]
	v_ashrrev_i32_e32 v23, 31, v22
	v_lshl_add_u64 v[2:3], v[22:23], 4, v[20:21]
	global_load_dwordx4 v[12:15], v[2:3], off
	v_or_b32_e32 v28, 0x200, v22
	v_ashrrev_i32_e32 v29, 31, v28
	v_lshl_add_u64 v[2:3], v[28:29], 4, v[20:21]
	global_load_dwordx4 v[16:19], v[2:3], off
	v_or_b32_e32 v184, 0x400, v22
	v_ashrrev_i32_e32 v185, 31, v184
	v_lshl_add_u64 v[184:185], v[184:185], 4, v[20:21]
	v_or_b32_e32 v188, 0x600, v22
	v_ashrrev_i32_e32 v189, 31, v188
	v_lshl_add_u64 v[188:189], v[188:189], 4, v[20:21]
	global_load_dwordx4 v[184:187], v[184:185], off
	global_load_dwordx4 v[188:191], v[188:189], off
	v_lshrrev_b32_e32 v99, 6, v0
	v_and_b32_e32 v98, 63, v0
	v_lshlrev_b32_e32 v118, 13, v99
	v_lshl_or_b32 v58, v98, 5, v118
	s_movk_i32 s15, 0x1000
	v_lshl_add_u64 v[24:25], s[6:7], 0, v[58:59]
	v_or_b32_e32 v32, 0x400, v22
	v_or_b32_e32 v62, 0x600, v22
	v_add_co_u32_e32 v64, vcc, s15, v24
	s_mov_b64 s[12:13], 0x1000
	s_mov_b64 s[16:17], 0x1800
	v_lshlrev_b32_e32 v72, 1, v60
	v_lshrrev_b32_e32 v23, 5, v22
	v_and_b32_e32 v34, 32, v22
	v_ashrrev_i32_e32 v33, 31, v32
	v_ashrrev_i32_e32 v63, 31, v62
	v_addc_co_u32_e32 v65, vcc, 0, v25, vcc
	global_load_dwordx4 v[6:9], v58, s[6:7] offset:16
	global_load_dwordx4 v[2:5], v58, s[6:7]
	global_load_dwordx4 v[54:57], v58, s[6:7] offset:2064
	global_load_dwordx4 v[50:53], v58, s[6:7] offset:2048
	v_lshrrev_b32_e32 v58, 6, v22
	v_bfe_u32 v73, v22, 8, 2
	v_lshl_add_u64 v[26:27], v[24:25], 0, s[12:13]
	v_lshl_add_u64 v[24:25], v[24:25], 0, s[16:17]
	v_cmp_ne_u32_e32 vcc, 0, v34
	v_sub_u32_e32 v75, v23, v72
	global_load_dwordx4 v[42:45], v[64:65], off
	global_load_dwordx4 v[46:49], v[26:27], off offset:16
	global_load_dwordx4 v[34:37], v[64:65], off offset:2048
	global_load_dwordx4 v[38:41], v[24:25], off offset:16
	v_mov_b32_e32 v61, 0x60
	v_cndmask_b32_e32 v74, 0, v61, vcc
	v_add_u32_e32 v33, v74, v58
	v_lshlrev_b32_e32 v64, 2, v33
	v_bfe_u32 v96, v0, 4, 1
	v_and_b32_e32 v100, 15, v0
	v_mov_b32_e32 v30, v59
	v_mov_b32_e32 v31, v59
	v_and_b32_e32 v64, 12, v64
	v_mul_u32_u24_e32 v29, 0xc000, v96
	v_bitop3_b32 v64, v64, v100, v73 bitop3:0x36
	v_lshl_or_b32 v64, v64, 4, v29
	v_lshlrev_b32_e32 v63, 1, v75
	v_lshl_add_u32 v33, v33, 8, v64
	v_bfe_u32 v71, v0, 1, 4
	v_and_b32_e32 v70, 32, v0
	v_lshlrev_b32_e32 v1, 3, v0
	v_lshrrev_b32_e32 v58, 1, v75
	v_and_b32_e32 v1, 8, v1
	v_add_lshl_u32 v58, v58, v70, 8
	v_lshlrev_b32_e32 v121, 3, v99
	v_bfe_u32 v101, v0, 4, 2
	v_lshlrev_b32_e32 v102, 2, v101
	v_and_b32_e32 v116, 31, v0
	v_bfe_u32 v119, v0, 5, 1
	v_lshlrev_b32_e32 v124, 1, v119
	v_lshlrev_b32_e32 v117, 8, v116
	v_lshrrev_b32_e32 v95, 4, v0
	s_movk_i32 s16, 0x60
	s_mov_b32 s17, 0xc000
	s_waitcnt vmcnt(11)
	v_fma_mix_f32 v200, v192, v12, 0 op_sel_hi:[0,1,0]
	v_fma_mix_f32 v201, v193, v12, 0 op_sel:[0,1,0] op_sel_hi:[0,1,0]
	v_fma_mix_f32 v200, v194, v13, v200 op_sel_hi:[0,1,0]
	v_fma_mix_f32 v201, v195, v13, v201 op_sel:[0,1,0] op_sel_hi:[0,1,0]
	v_fma_mix_f32 v200, v196, v14, v200 op_sel_hi:[0,1,0]
	v_fma_mix_f32 v201, v197, v14, v201 op_sel:[0,1,0] op_sel_hi:[0,1,0]
	v_fma_mix_f32 v200, v198, v15, v200 op_sel_hi:[0,1,0]
	v_fma_mix_f32 v201, v199, v15, v201 op_sel:[0,1,0] op_sel_hi:[0,1,0]
	v_cvt_f32_f16_e32 v65, v12
	v_cvt_f32_f16_sdwa v66, v12 dst_sel:DWORD dst_unused:UNUSED_PAD src0_sel:WORD_1
	v_cvt_f32_f16_e32 v69, v14
	v_cvt_f32_f16_sdwa v74, v14 dst_sel:DWORD dst_unused:UNUSED_PAD src0_sel:WORD_1
	v_cvt_f32_f16_e32 v67, v13
	v_cvt_f32_f16_sdwa v68, v13 dst_sel:DWORD dst_unused:UNUSED_PAD src0_sel:WORD_1
	v_cvt_f32_f16_e32 v76, v15
	v_cvt_f32_f16_sdwa v77, v15 dst_sel:DWORD dst_unused:UNUSED_PAD src0_sel:WORD_1
	v_cvt_pk_fp8_f32 v30, v65, v66
	v_cvt_pk_fp8_f32 v31, v69, v74
	ds_write_b128 v33, v[12:15]
	v_and_b32_e32 v12, 12, v63
	v_bfe_u32 v13, v75, 3, 2
	v_cvt_pk_fp8_f32 v30, v67, v68 op_sel:[0,0,1]
	v_cvt_pk_fp8_f32 v31, v76, v77 op_sel:[0,0,1]
	v_bitop3_b32 v12, v12, v71, v13 bitop3:0x36
	v_lshlrev_b32_e32 v12, 4, v12
	v_or3_b32 v12, v58, v12, v1
	v_add_u32_e32 v12, 0x23800, v12
	ds_write_b64 v12, v[30:31]
	v_and_b32_e32 v12, 32, v28
	v_cmp_ne_u32_e32 vcc, 0, v12
	v_lshrrev_b32_e32 v13, 6, v28
	v_bfe_u32 v15, v28, 8, 2
	v_cndmask_b32_e32 v12, 0, v61, vcc
	v_add_u32_e32 v12, v12, v13
	v_lshlrev_b32_e32 v13, 2, v12
	v_and_b32_e32 v13, 12, v13
	v_bitop3_b32 v13, v13, v100, v15 bitop3:0x36
	v_lshl_or_b32 v13, v13, 4, v29
	v_lshl_add_u32 v12, v12, 8, v13
	s_waitcnt vmcnt(10)
	v_fma_mix_f32 v202, v192, v16, 0 op_sel_hi:[0,1,0]
	v_fma_mix_f32 v203, v193, v16, 0 op_sel:[0,1,0] op_sel_hi:[0,1,0]
	v_fma_mix_f32 v202, v194, v17, v202 op_sel_hi:[0,1,0]
	v_fma_mix_f32 v203, v195, v17, v203 op_sel:[0,1,0] op_sel_hi:[0,1,0]
	v_fma_mix_f32 v202, v196, v18, v202 op_sel_hi:[0,1,0]
	v_fma_mix_f32 v203, v197, v18, v203 op_sel:[0,1,0] op_sel_hi:[0,1,0]
	v_fma_mix_f32 v202, v198, v19, v202 op_sel_hi:[0,1,0]
	v_fma_mix_f32 v203, v199, v19, v203 op_sel:[0,1,0] op_sel_hi:[0,1,0]
	v_cvt_f32_f16_e32 v13, v16
	v_cvt_f32_f16_sdwa v15, v16 dst_sel:DWORD dst_unused:UNUSED_PAD src0_sel:WORD_1
	ds_write_b128 v12, v[16:19]
	v_mov_b32_e32 v12, v59
	v_cvt_f32_f16_e32 v16, v17
	v_cvt_pk_fp8_f32 v12, v13, v15
	v_cvt_f32_f16_e32 v15, v18
	v_cvt_f32_f16_sdwa v18, v18 dst_sel:DWORD dst_unused:UNUSED_PAD src0_sel:WORD_1
	v_cvt_f32_f16_sdwa v17, v17 dst_sel:DWORD dst_unused:UNUSED_PAD src0_sel:WORD_1
	v_mov_b32_e32 v13, v59
	v_lshrrev_b32_e32 v14, 5, v28
	v_cvt_f32_f16_e32 v28, v19
	v_cvt_f32_f16_sdwa v19, v19 dst_sel:DWORD dst_unused:UNUSED_PAD src0_sel:WORD_1
	v_cvt_pk_fp8_f32 v13, v15, v18
	v_sub_u32_e32 v14, v14, v72
	v_cvt_pk_fp8_f32 v12, v16, v17 op_sel:[0,0,1]
	v_lshlrev_b32_e32 v16, 1, v14
	v_lshrrev_b32_e32 v15, 1, v14
	v_and_b32_e32 v16, 12, v16
	v_bfe_u32 v14, v14, 3, 2
	v_cvt_pk_fp8_f32 v13, v28, v19 op_sel:[0,0,1]
	v_bitop3_b32 v14, v16, v71, v14 bitop3:0x36
	v_add_lshl_u32 v15, v15, v70, 8
	v_lshlrev_b32_e32 v14, 4, v14
	v_or3_b32 v14, v15, v14, v1
	v_add_u32_e32 v14, 0x23800, v14
	ds_write_b64 v14, v[12:13]
	v_and_b32_e32 v12, 32, v32
	v_cmp_ne_u32_e32 vcc, 0, v12
	v_lshrrev_b32_e32 v13, 6, v32
	s_waitcnt vmcnt(9)
	v_fma_mix_f32 v204, v192, v184, 0 op_sel_hi:[0,1,0]
	v_fma_mix_f32 v205, v193, v184, 0 op_sel:[0,1,0] op_sel_hi:[0,1,0]
	v_fma_mix_f32 v204, v194, v185, v204 op_sel_hi:[0,1,0]
	v_fma_mix_f32 v205, v195, v185, v205 op_sel:[0,1,0] op_sel_hi:[0,1,0]
	v_fma_mix_f32 v204, v196, v186, v204 op_sel_hi:[0,1,0]
	v_fma_mix_f32 v205, v197, v186, v205 op_sel:[0,1,0] op_sel_hi:[0,1,0]
	v_fma_mix_f32 v204, v198, v187, v204 op_sel_hi:[0,1,0]
	v_fma_mix_f32 v205, v199, v187, v205 op_sel:[0,1,0] op_sel_hi:[0,1,0]
	v_cvt_f32_f16_sdwa v15, v184 dst_sel:DWORD dst_unused:UNUSED_PAD src0_sel:WORD_1
	v_cndmask_b32_e32 v12, 0, v61, vcc
	v_add_u32_e32 v12, v12, v13
	v_lshlrev_b32_e32 v13, 2, v12
	v_and_b32_e32 v13, 12, v13
	v_bitop3_b32 v13, v13, v100, v73 bitop3:0x36
	v_lshl_or_b32 v13, v13, 4, v29
	v_lshl_add_u32 v12, v12, 8, v13
	v_cvt_f32_f16_e32 v13, v184
	ds_write_b128 v12, v[184:187]
	v_mov_b32_e32 v12, v59
	v_cvt_f32_f16_sdwa v18, v186 dst_sel:DWORD dst_unused:UNUSED_PAD src0_sel:WORD_1
	v_cvt_pk_fp8_f32 v12, v13, v15
	v_cvt_f32_f16_e32 v15, v186
	v_cvt_f32_f16_e32 v16, v185
	v_cvt_f32_f16_sdwa v17, v185 dst_sel:DWORD dst_unused:UNUSED_PAD src0_sel:WORD_1
	v_mov_b32_e32 v13, v59
	v_lshrrev_b32_e32 v14, 5, v32
	v_cvt_f32_f16_e32 v19, v187
	v_cvt_f32_f16_sdwa v20, v187 dst_sel:DWORD dst_unused:UNUSED_PAD src0_sel:WORD_1
	v_cvt_pk_fp8_f32 v13, v15, v18
	v_sub_u32_e32 v14, v14, v72
	v_cvt_pk_fp8_f32 v12, v16, v17 op_sel:[0,0,1]
	v_lshlrev_b32_e32 v16, 1, v14
	v_lshrrev_b32_e32 v15, 1, v14
	v_and_b32_e32 v16, 12, v16
	v_bfe_u32 v14, v14, 3, 2
	v_cvt_pk_fp8_f32 v13, v19, v20 op_sel:[0,0,1]
	v_bitop3_b32 v14, v16, v71, v14 bitop3:0x36
	v_add_lshl_u32 v15, v15, v70, 8
	v_lshlrev_b32_e32 v14, 4, v14
	v_or3_b32 v14, v15, v14, v1
	v_add_u32_e32 v14, 0x23800, v14
	ds_write_b64 v14, v[12:13]
	v_and_b32_e32 v12, 32, v62
	v_cmp_ne_u32_e32 vcc, 0, v12
	v_lshrrev_b32_e32 v13, 6, v62
	v_bfe_u32 v15, v62, 8, 2
	v_cndmask_b32_e32 v12, 0, v61, vcc
	v_add_u32_e32 v12, v12, v13
	v_lshlrev_b32_e32 v13, 2, v12
	v_and_b32_e32 v13, 12, v13
	v_bitop3_b32 v13, v13, v100, v15 bitop3:0x36
	v_lshl_or_b32 v13, v13, 4, v29
	v_lshl_add_u32 v12, v12, 8, v13
	s_waitcnt vmcnt(8)
	v_fma_mix_f32 v206, v192, v188, 0 op_sel_hi:[0,1,0]
	v_fma_mix_f32 v207, v193, v188, 0 op_sel:[0,1,0] op_sel_hi:[0,1,0]
	v_fma_mix_f32 v206, v194, v189, v206 op_sel_hi:[0,1,0]
	v_fma_mix_f32 v207, v195, v189, v207 op_sel:[0,1,0] op_sel_hi:[0,1,0]
	v_fma_mix_f32 v206, v196, v190, v206 op_sel_hi:[0,1,0]
	v_fma_mix_f32 v207, v197, v190, v207 op_sel:[0,1,0] op_sel_hi:[0,1,0]
	v_fma_mix_f32 v206, v198, v191, v206 op_sel_hi:[0,1,0]
	v_fma_mix_f32 v207, v199, v191, v207 op_sel:[0,1,0] op_sel_hi:[0,1,0]
	v_cvt_f32_f16_e32 v13, v188
	v_cvt_f32_f16_sdwa v15, v188 dst_sel:DWORD dst_unused:UNUSED_PAD src0_sel:WORD_1
	ds_write_b128 v12, v[188:191]
	v_mov_b32_e32 v12, v59
	v_cvt_f32_f16_sdwa v18, v190 dst_sel:DWORD dst_unused:UNUSED_PAD src0_sel:WORD_1
	v_cvt_pk_fp8_f32 v12, v13, v15
	v_cvt_f32_f16_e32 v15, v190
	v_cvt_f32_f16_e32 v16, v189
	v_cvt_f32_f16_sdwa v17, v189 dst_sel:DWORD dst_unused:UNUSED_PAD src0_sel:WORD_1
	v_mov_b32_e32 v13, v59
	v_lshrrev_b32_e32 v14, 5, v62
	v_cvt_f32_f16_e32 v19, v191
	v_cvt_f32_f16_sdwa v20, v191 dst_sel:DWORD dst_unused:UNUSED_PAD src0_sel:WORD_1
	v_cvt_pk_fp8_f32 v13, v15, v18
	v_sub_u32_e32 v14, v14, v72
	v_cvt_pk_fp8_f32 v12, v16, v17 op_sel:[0,0,1]
	v_lshlrev_b32_e32 v16, 1, v14
	v_lshrrev_b32_e32 v15, 1, v14
	v_and_b32_e32 v16, 12, v16
	v_bfe_u32 v14, v14, 3, 2
	v_cvt_pk_fp8_f32 v13, v19, v20 op_sel:[0,0,1]
	v_bitop3_b32 v14, v16, v71, v14 bitop3:0x36
	v_add_lshl_u32 v15, v15, v70, 8
	v_lshlrev_b32_e32 v14, 4, v14
	v_or3_b32 v14, v15, v14, v1
	v_add_u32_e32 v14, 0x23800, v14
	v_add_f32_e32 v200, v200, v201
	v_add_f32_e32 v202, v202, v203
	v_add_f32_e32 v204, v204, v205
	v_add_f32_e32 v206, v206, v207
	v_lshlrev_b32_e32 v208, 7, v119
	v_lshl_add_u32 v208, v99, 2, v208
	v_add_u32_e32 v208, 0x27800, v208
	v_add_f32_dpp v200, v200, v200 quad_perm:[1,0,3,2] row_mask:0xf bank_mask:0xf
	v_add_f32_dpp v202, v202, v202 quad_perm:[1,0,3,2] row_mask:0xf bank_mask:0xf
	v_add_f32_dpp v204, v204, v204 quad_perm:[1,0,3,2] row_mask:0xf bank_mask:0xf
	v_add_f32_dpp v206, v206, v206 quad_perm:[1,0,3,2] row_mask:0xf bank_mask:0xf
	v_add_f32_dpp v200, v200, v200 quad_perm:[2,3,0,1] row_mask:0xf bank_mask:0xf
	v_add_f32_dpp v202, v202, v202 quad_perm:[2,3,0,1] row_mask:0xf bank_mask:0xf
	v_add_f32_dpp v204, v204, v204 quad_perm:[2,3,0,1] row_mask:0xf bank_mask:0xf
	v_add_f32_dpp v206, v206, v206 quad_perm:[2,3,0,1] row_mask:0xf bank_mask:0xf
	v_add_f32_dpp v200, v200, v200 row_half_mirror row_mask:0xf bank_mask:0xf
	v_add_f32_dpp v202, v202, v202 row_half_mirror row_mask:0xf bank_mask:0xf
	v_add_f32_dpp v204, v204, v204 row_half_mirror row_mask:0xf bank_mask:0xf
	v_add_f32_dpp v206, v206, v206 row_half_mirror row_mask:0xf bank_mask:0xf
	v_add_f32_dpp v200, v200, v200 row_mirror row_mask:0xf bank_mask:0xf
	v_add_f32_dpp v202, v202, v202 row_mirror row_mask:0xf bank_mask:0xf
	v_add_f32_dpp v204, v204, v204 row_mirror row_mask:0xf bank_mask:0xf
	v_add_f32_dpp v206, v206, v206 row_mirror row_mask:0xf bank_mask:0xf
	v_add_f32_dpp v200, v200, v200 row_bcast:15 row_mask:0xa bank_mask:0xf
	v_add_f32_dpp v202, v202, v202 row_bcast:15 row_mask:0xa bank_mask:0xf
	v_add_f32_dpp v204, v204, v204 row_bcast:15 row_mask:0xa bank_mask:0xf
	v_add_f32_dpp v206, v206, v206 row_bcast:15 row_mask:0xa bank_mask:0xf
	s_mov_b32 exec_lo, 0xffff0000
	s_mov_b32 exec_hi, 0xffff0000
	ds_write_b32 v208, v200
	ds_write_b32 v208, v202 offset:32
	ds_write_b32 v208, v204 offset:64
	ds_write_b32 v208, v206 offset:96
	s_mov_b64 exec, -1
	v_cmp_lt_i32_e32 vcc, v121, v60
	ds_write_b64 v14, v[12:13]
	v_mov_b32_e32 v15, v59
	v_cndmask_b32_e64 v12, 32, 0, vcc
	v_add_u32_e32 v16, v12, v121
	v_or_b32_e32 v12, v16, v101
	v_lshlrev_b32_e32 v58, 1, v12
	v_lshrrev_b32_e32 v12, 5, v0
	v_and_b32_e32 v12, 2, v12
	v_bitop3_b32 v14, v102, v100, v12 bitop3:0x36
	v_lshl_add_u64 v[12:13], v[10:11], 0, v[58:59]
	v_lshlrev_b64 v[12:13], 9, v[12:13]
	v_lshlrev_b32_e32 v16, 8, v16
	v_lshl_add_u64 v[12:13], s[4:5], 0, v[12:13]
	v_lshlrev_b32_e32 v14, 4, v14
	v_readfirstlane_b32 s6, v16
	v_add_u32_e32 v17, 0xc000, v16
	v_lshl_add_u64 v[12:13], v[12:13], 0, v[14:15]
	s_mov_b32 m0, s6
	s_mov_b64 s[6:7], 0x100
	v_readfirstlane_b32 s12, v17
	global_load_lds_dwordx4 v[12:13], off
	v_lshl_add_u64 v[12:13], v[12:13], 0, s[6:7]
	s_mov_b32 m0, s12
	v_or_b32_e32 v58, 1, v58
	global_load_lds_dwordx4 v[12:13], off
	v_lshl_add_u64 v[12:13], v[10:11], 0, v[58:59]
	v_lshlrev_b64 v[12:13], 9, v[12:13]
	v_lshl_add_u64 v[12:13], s[4:5], 0, v[12:13]
	v_lshl_add_u64 v[12:13], v[12:13], 0, v[14:15]
	v_add_u32_e32 v14, 0x6000, v16
	v_bfe_u32 v61, v0, 2, 2
	v_readfirstlane_b32 s12, v14
	v_add_u32_e32 v14, 0x12000, v16
	s_mov_b32 m0, s12
	v_readfirstlane_b32 s12, v14
	global_load_lds_dwordx4 v[12:13], off
	v_lshl_add_u64 v[12:13], v[12:13], 0, s[6:7]
	s_mov_b32 m0, s12
	v_add_u32_e32 v18, 0x23800, v117
	global_load_lds_dwordx4 v[12:13], off
	v_or_b32_e32 v12, 4, v121
	v_cmp_lt_i32_e32 vcc, v12, v60
	s_nop 1
	v_cndmask_b32_e64 v13, 32, 0, vcc
	v_add_u32_e32 v16, v13, v12
	v_or_b32_e32 v13, v16, v101
	v_lshlrev_b32_e32 v58, 1, v13
	v_bfe_u32 v12, v12, 2, 2
	v_bitop3_b32 v14, v102, v100, v12 bitop3:0x36
	v_lshl_add_u64 v[12:13], v[10:11], 0, v[58:59]
	v_lshlrev_b64 v[12:13], 9, v[12:13]
	v_lshlrev_b32_e32 v16, 8, v16
	v_lshl_add_u64 v[12:13], s[4:5], 0, v[12:13]
	v_lshlrev_b32_e32 v14, 4, v14
	v_readfirstlane_b32 s12, v16
	v_add_u32_e32 v17, 0xc000, v16
	v_lshl_add_u64 v[12:13], v[12:13], 0, v[14:15]
	s_mov_b32 m0, s12
	v_readfirstlane_b32 s12, v17
	v_or_b32_e32 v58, 1, v58
	global_load_lds_dwordx4 v[12:13], off
	v_lshl_add_u64 v[12:13], v[12:13], 0, s[6:7]
	s_mov_b32 m0, s12
	v_lshl_add_u64 v[10:11], v[10:11], 0, v[58:59]
	global_load_lds_dwordx4 v[12:13], off
	v_lshlrev_b64 v[10:11], 9, v[10:11]
	v_add_u32_e32 v12, 0x6000, v16
	v_lshl_add_u64 v[10:11], s[4:5], 0, v[10:11]
	v_readfirstlane_b32 s4, v12
	v_add_u32_e32 v12, 0x12000, v16
	v_lshl_add_u64 v[10:11], v[10:11], 0, v[14:15]
	s_mov_b32 m0, s4
	v_readfirstlane_b32 s4, v12
	global_load_lds_dwordx4 v[10:11], off
	v_lshl_add_u64 v[10:11], v[10:11], 0, s[6:7]
	s_mov_b32 m0, s4
	s_nop 0
	global_load_lds_dwordx4 v[10:11], off
	s_waitcnt lgkmcnt(0)
	s_barrier
	v_lshlrev_b32_e32 v10, 2, v0
	v_and_b32_e32 v94, 12, v10
	v_or_b32_e32 v120, v94, v61
	v_bitop3_b32 v10, v124, v94, v61 bitop3:0x1e
	v_lshl_or_b32 v14, v10, 4, v18
	v_bitop3_b32 v10, v124, v120, 1 bitop3:0x36
	v_lshl_or_b32 v19, v10, 4, v18
	s_load_dwordx4 s[4:7], s[0:1], 0x20
	s_load_dwordx2 s[12:13], s[0:1], 0x38
	ds_read_b128 v[10:13], v14
	ds_read_b128 v[62:65], v14 offset:8192
	ds_read_b128 v[14:17], v19
	ds_read_b128 v[66:69], v19 offset:8192
	v_bitop3_b32 v19, v124, v120, 4 bitop3:0x36
	v_lshl_or_b32 v19, v19, 4, v18
	v_bitop3_b32 v20, v124, v120, 5 bitop3:0x36
	v_lshl_or_b32 v20, v20, 4, v18
	ds_read_b128 v[70:73], v19
	ds_read_b128 v[78:81], v19 offset:8192
	ds_read_b128 v[74:77], v20
	ds_read_b128 v[82:85], v20 offset:8192
	v_bitop3_b32 v19, v124, v120, 8 bitop3:0x36
	v_lshl_or_b32 v19, v19, 4, v18
	v_bitop3_b32 v20, v124, v120, 9 bitop3:0x36
	v_lshl_or_b32 v20, v20, 4, v18
	ds_read_b128 v[86:89], v19
	ds_read_b128 v[104:107], v19 offset:8192
	ds_read_b128 v[90:93], v20
	ds_read_b128 v[108:111], v20 offset:8192
	v_bitop3_b32 v19, v124, v120, 12 bitop3:0x36
	v_lshl_or_b32 v19, v19, 4, v18
	v_bitop3_b32 v20, v124, v120, 13 bitop3:0x36
	v_lshl_or_b32 v18, v20, 4, v18
	ds_read_b128 v[126:129], v19
	ds_read_b128 v[134:137], v19 offset:8192
	ds_read_b128 v[130:133], v18
	ds_read_b128 v[138:141], v18 offset:8192
	v_mov_b32_e32 v103, 0x7f
	v_lshlrev_b32_e32 v58, 7, v99
	v_or_b32_e32 v122, 0x18000, v117
	s_waitcnt vmcnt(8) lgkmcnt(0)
	v_mfma_scale_f32_32x32x64_f8f6f4 v[18:33], v[2:9], v[10:17], 0, v103, v103 op_sel_hi:[0,0,0]
	v_lshlrev_b32_e32 v125, 3, v119
	v_or_b32_e32 v123, 0x1a000, v117
	v_mfma_scale_f32_32x32x64_f8f6f4 v[2:17], v[2:9], v[62:69], 0, v103, v103 op_sel_hi:[0,0,0]
	v_and_b32_e32 v62, 12, v95
	v_mfma_scale_f32_32x32x64_f8f6f4 v[18:33], v[50:57], v[70:77], v[18:33], v103, v103 op_sel_hi:[0,0,0]
	v_mfma_scale_f32_32x32x64_f8f6f4 v[2:17], v[50:57], v[78:85], v[2:17], v103, v103 op_sel_hi:[0,0,0]
	v_lshl_add_u64 v[50:51], s[10:11], 0, v[58:59]
	v_lshlrev_b32_e32 v58, 4, v119
	v_lshl_add_u64 v[54:55], v[50:51], 0, v[58:59]
	global_load_dwordx4 v[50:53], v[54:55], off
	s_brev_b32 s10, 60
	v_lshlrev_b32_e32 v58, 6, v0
	v_and_b32_e32 v58, 0x4000, v58
	v_or3_b32 v63, v122, v58, v125
	v_or3_b32 v58, v123, v58, v125
	v_mfma_scale_f32_32x32x64_f8f6f4 v[18:33], v[42:49], v[86:93], v[18:33], v103, v103 op_sel_hi:[0,0,0]
	v_mfma_scale_f32_32x32x64_f8f6f4 v[2:17], v[42:49], v[104:111], v[2:17], v103, v103 op_sel_hi:[0,0,0]
	global_load_dwordx4 v[42:45], v[54:55], off offset:32
	global_load_dwordx4 v[46:49], v[54:55], off offset:64
	s_nop 0
	global_load_dwordx4 v[54:57], v[54:55], off offset:96
	v_mfma_scale_f32_32x32x64_f8f6f4 v[2:17], v[34:41], v[134:141], v[2:17], v103, v103 op_sel_hi:[0,0,0]
	v_mfma_scale_f32_32x32x64_f8f6f4 v[18:33], v[34:41], v[126:133], v[18:33], v103, v103 op_sel_hi:[0,0,0]
	v_lshlrev_b32_e32 v250, 14, v99
	v_lshl_or_b32 v250, v98, 4, v250
	v_add_u32_e32 v251, 0x1000, v250
	v_add_u32_e32 v252, 0x2000, v250
	v_add_u32_e32 v253, 0x3000, v250
	global_load_dwordx4 v[184:187], v250, s[8:9]
	global_load_dwordx4 v[188:191], v250, s[8:9] offset:1024
	global_load_dwordx4 v[192:195], v250, s[8:9] offset:2048
	global_load_dwordx4 v[196:199], v250, s[8:9] offset:3072
	global_load_dwordx4 v[200:203], v251, s[8:9]
	global_load_dwordx4 v[204:207], v251, s[8:9] offset:1024
	global_load_dwordx4 v[208:211], v251, s[8:9] offset:2048
	global_load_dwordx4 v[212:215], v251, s[8:9] offset:3072
	global_load_dwordx4 v[216:219], v252, s[8:9]
	global_load_dwordx4 v[220:223], v252, s[8:9] offset:1024
	global_load_dwordx4 v[224:227], v252, s[8:9] offset:2048
	global_load_dwordx4 v[228:231], v252, s[8:9] offset:3072
	global_load_dwordx4 v[232:235], v253, s[8:9]
	global_load_dwordx4 v[236:239], v253, s[8:9] offset:1024
	global_load_dwordx4 v[240:243], v253, s[8:9] offset:2048
	global_load_dwordx4 v[244:247], v253, s[8:9] offset:3072
	s_waitcnt vmcnt(16)
	s_nop 15
	s_nop 1
	v_fma_f32 v2, v2, s10, v50
	v_fma_f32 v3, v3, s10, v51
	v_fma_f32 v4, v4, s10, v52
	v_fma_f32 v5, v5, s10, v53
	v_cvt_pk_f16_f32 v2, v2, v3
	v_cvt_pk_f16_f32 v3, v4, v5
	v_bitop3_b32 v4, v95, v120, 12 bitop3:0x6c
	v_pk_fma_f32 v[18:19], v[18:19], s[10:11], v[50:51] op_sel_hi:[1,0,1]
	v_pk_fma_f32 v[20:21], v[20:21], s[10:11], v[52:53] op_sel_hi:[1,0,1]
	v_lshlrev_b32_e32 v4, 4, v4
	v_cvt_pk_f16_f32 v18, v18, v19
	v_cvt_pk_f16_f32 v19, v20, v21
	v_or_b32_e32 v5, v63, v4
	v_or_b32_e32 v4, v58, v4
	ds_write_b64 v5, v[18:19]
	ds_write_b64 v4, v[2:3]
	v_pk_fma_f32 v[2:3], v[22:23], s[10:11], v[42:43] op_sel_hi:[1,0,1]
	v_pk_fma_f32 v[4:5], v[6:7], s[10:11], v[42:43] op_sel_hi:[1,0,1]
	v_pk_fma_f32 v[6:7], v[24:25], s[10:11], v[44:45] op_sel_hi:[1,0,1]
	v_cvt_pk_f16_f32 v2, v2, v3
	v_cvt_pk_f16_f32 v3, v6, v7
	v_pk_fma_f32 v[6:7], v[8:9], s[10:11], v[44:45] op_sel_hi:[1,0,1]
	v_cvt_pk_f16_f32 v4, v4, v5
	v_cvt_pk_f16_f32 v5, v6, v7
	v_bitop3_b32 v6, v62, v120, 1 bitop3:0x36
	v_lshlrev_b32_e32 v6, 4, v6
	v_or_b32_e32 v7, v63, v6
	ds_write_b64 v7, v[2:3]
	v_or_b32_e32 v2, v58, v6
	ds_write_b64 v2, v[4:5]
	v_pk_fma_f32 v[2:3], v[26:27], s[10:11], v[46:47] op_sel_hi:[1,0,1]
	v_pk_fma_f32 v[6:7], v[28:29], s[10:11], v[48:49] op_sel_hi:[1,0,1]
	v_cvt_pk_f16_f32 v2, v2, v3
	v_pk_fma_f32 v[4:5], v[10:11], s[10:11], v[46:47] op_sel_hi:[1,0,1]
	v_cvt_pk_f16_f32 v3, v6, v7
	v_pk_fma_f32 v[6:7], v[12:13], s[10:11], v[48:49] op_sel_hi:[1,0,1]
	v_cvt_pk_f16_f32 v4, v4, v5
	v_cvt_pk_f16_f32 v5, v6, v7
	v_bitop3_b32 v6, v62, v120, 2 bitop3:0x36
	v_lshlrev_b32_e32 v6, 4, v6
	v_or_b32_e32 v7, v63, v6
	ds_write_b64 v7, v[2:3]
	v_or_b32_e32 v2, v58, v6
	ds_write_b64 v2, v[4:5]
	v_pk_fma_f32 v[2:3], v[30:31], s[10:11], v[54:55] op_sel_hi:[1,0,1]
	v_pk_fma_f32 v[6:7], v[32:33], s[10:11], v[56:57] op_sel_hi:[1,0,1]
	v_cvt_pk_f16_f32 v2, v2, v3
	v_pk_fma_f32 v[4:5], v[14:15], s[10:11], v[54:55] op_sel_hi:[1,0,1]
	v_cvt_pk_f16_f32 v3, v6, v7
	v_pk_fma_f32 v[6:7], v[16:17], s[10:11], v[56:57] op_sel_hi:[1,0,1]
	v_cvt_pk_f16_f32 v4, v4, v5
	v_cvt_pk_f16_f32 v5, v6, v7
	v_bitop3_b32 v6, v62, v120, 3 bitop3:0x36
	v_lshlrev_b32_e32 v6, 4, v6
	v_or_b32_e32 v7, v63, v6
	ds_write_b64 v7, v[2:3]
	v_or_b32_e32 v2, v58, v6
	ds_write_b64 v2, v[4:5]
	v_lshlrev_b32_e32 v2, 8, v101
	s_waitcnt lgkmcnt(0)
	s_barrier
	v_lshrrev_b32_e32 v27, 8, v0
	v_lshrrev_b32_e32 v3, 3, v0
	v_and_b32_e32 v3, 16, v3
	v_mul_u32_u24_e32 v28, 0x60, v27
	v_lshlrev_b32_e32 v26, 5, v27
	v_or_b32_e32 v146, v3, v100
	v_or_b32_e32 v147, v28, v100
	v_or_b32_e32 v4, v146, v26
	v_lshlrev_b32_e32 v248, 2, v4
	v_add_u32_e32 v248, 0x27800, v248
	v_or_b32_e32 v3, v147, v3
	v_lshlrev_b32_e32 v4, 8, v4
	v_add_u32_e32 v3, v3, v60
	v_or_b32_e32 v5, 0x18000, v4
	v_bitop3_b32 v11, v101, v120, 12 bitop3:0x36
	v_or_b32_e32 v95, 0x1c000, v4
	v_lshlrev_b32_e32 v29, 3, v101
	v_lshlrev_b32_e32 v4, 8, v3
	v_lshlrev_b32_e32 v12, 2, v3
	v_bfe_u32 v3, v3, 2, 2
	v_bitop3_b32 v6, v101, v94, v61 bitop3:0x1e
	v_bitop3_b32 v8, v101, v120, 4 bitop3:0x36
	v_bitop3_b32 v10, v101, v120, 8 bitop3:0x36
	v_lshlrev_b32_e32 v94, 4, v11
	v_and_b32_e32 v11, 8, v29
	v_and_or_b32 v3, v12, 12, v3
	v_lshlrev_b32_e32 v6, 4, v6
	v_lshlrev_b32_e32 v8, 4, v8
	v_lshlrev_b32_e32 v58, 4, v10
	v_mad_u32_u24 v4, v119, s17, v4
	v_bitop3_b32 v12, v11, v3, 1 bitop3:0x36
	v_bitop3_b32 v13, v11, v3, 2 bitop3:0x36
	v_bitop3_b32 v14, v11, v3, 3 bitop3:0x36
	v_bitop3_b32 v15, v11, v3, 4 bitop3:0x36
	v_bitop3_b32 v16, v11, v3, 5 bitop3:0x36
	v_bitop3_b32 v17, v11, v3, 6 bitop3:0x36
	v_or_b32_e32 v7, v5, v6
	v_or_b32_e32 v9, v5, v8
	v_or_b32_e32 v10, v5, v58
	v_or_b32_e32 v5, v5, v94
	v_or_b32_e32 v6, v95, v6
	v_or_b32_e32 v60, v95, v8
	v_bitop3_b32 v8, v29, v3, 8 bitop3:0x6c
	v_bitop3_b32 v2, v11, v3, 7 bitop3:0x36
	v_lshl_or_b32 v112, v12, 4, v4
	v_lshl_or_b32 v126, v13, 4, v4
	v_lshl_or_b32 v130, v14, 4, v4
	v_lshl_or_b32 v134, v15, 4, v4
	v_lshl_or_b32 v138, v16, 4, v4
	v_lshl_or_b32 v142, v17, 4, v4
	v_lshl_or_b32 v103, v8, 4, v4
	v_lshl_or_b32 v148, v2, 4, v4
	ds_read_b128 v[22:25], v7
	ds_read_b128 v[18:21], v9
	ds_read_b128 v[14:17], v10
	ds_read_b128 v[10:13], v5
	ds_read_b128 v[6:9], v6
	ds_read_b128 v[2:5], v60
	v_bfe_u32 v103, v0, 6, 1
	s_movk_i32 s5, 0x2000
	v_mbcnt_lo_u32_b32 v30, -1, 0
	v_mbcnt_hi_u32_b32 v32, -1, v30
	v_and_b32_e32 v33, 64, v32
	v_xor_b32_e32 v30, 16, v32
	v_add_u32_e32 v33, 64, v33
	v_cmp_lt_i32_e32 vcc, v30, v33
	v_mad_u32_u24 v44, v103, 48, v147
	v_lshlrev_b32_e32 v60, 8, v44
	v_cndmask_b32_e32 v30, v32, v30, vcc
	v_lshlrev_b32_e32 v30, 2, v30
	v_lshlrev_b32_e32 v44, 2, v44
	v_or_b32_e32 v35, v95, v58
	v_lshlrev_b32_e32 v58, 14, v99
	v_and_b32_e32 v44, 12, v44
	v_xor_b32_e32 v31, 32, v32
	v_cmp_lt_i32_e32 vcc, v31, v33
	v_or_b32_e32 v56, v44, v61
	v_bitop3_b32 v44, v101, v44, v61 bitop3:0x1e
	v_cndmask_b32_e32 v31, v32, v31, vcc
	v_lshl_add_u64 v[32:33], s[8:9], 0, v[58:59]
	v_lshlrev_b32_e32 v58, 4, v98
	v_or_b32_e32 v36, v95, v94
	v_lshl_add_u64 v[88:89], v[32:33], 0, v[58:59]
	v_lshl_or_b32 v57, v44, 4, v60
	ds_read_b128 v[40:43], v35
	ds_read_b128 v[106:109], v36
	s_load_dword s4, s[6:7], 0x0
	ds_read_b128 v[44:47], v57
	v_bitop3_b32 v48, v101, v56, 4 bitop3:0x36
	v_lshl_or_b32 v62, v48, 4, v60
	ds_read_b128 v[48:51], v62
	v_bitop3_b32 v52, v101, v56, 8 bitop3:0x36
	v_lshl_or_b32 v63, v52, 4, v60
	ds_read_b128 v[52:55], v63
	s_waitcnt lgkmcnt(0)
	v_mfma_f32_16x16x32_f16 v[44:47], v[44:47], v[22:25], 0
	v_bitop3_b32 v64, v101, v56, 12 bitop3:0x36
	ds_read_b128 v[56:59], v57 offset:49152
	v_lshl_or_b32 v60, v64, 4, v60
	v_mfma_f32_16x16x32_f16 v[44:47], v[48:51], v[18:21], v[44:47]
	ds_read_b128 v[68:71], v60
	ds_read_b128 v[72:75], v62 offset:49152
	v_mad_u32_u24 v104, v103, 3, 1
	v_lshlrev_b32_e32 v132, 4, v104
	v_mfma_f32_16x16x32_f16 v[44:47], v[52:55], v[14:17], v[44:47]
	v_add_u32_e32 v52, v132, v147
	ds_read_b128 v[76:79], v63 offset:49152
	ds_read_b128 v[80:83], v60 offset:49152
	s_waitcnt lgkmcnt(3)
	v_mfma_f32_16x16x32_f16 v[44:47], v[68:71], v[10:13], v[44:47]
	v_lshlrev_b32_e32 v60, 8, v52
	v_lshlrev_b32_e32 v52, 2, v52
	v_and_b32_e32 v52, 12, v52
	v_mfma_f32_16x16x32_f16 v[44:47], v[56:59], v[6:9], v[44:47]
	v_or_b32_e32 v62, v52, v61
	v_bitop3_b32 v52, v101, v52, v61 bitop3:0x1e
	v_lshl_or_b32 v63, v52, 4, v60
	s_waitcnt lgkmcnt(2)
	v_mfma_f32_16x16x32_f16 v[44:47], v[72:75], v[2:5], v[44:47]
	ds_read_b128 v[52:55], v63
	v_bitop3_b32 v56, v101, v62, 4 bitop3:0x36
	v_lshl_or_b32 v84, v56, 4, v60
	s_waitcnt lgkmcnt(2)
	v_mfma_f32_16x16x32_f16 v[44:47], v[76:79], v[40:43], v[44:47]
	ds_read_b128 v[56:59], v84
	v_bitop3_b32 v68, v101, v62, 8 bitop3:0x36
	v_lshl_or_b32 v85, v68, 4, v60
	s_waitcnt lgkmcnt(2)
	v_mfma_f32_16x16x32_f16 v[110:113], v[80:83], v[106:109], v[44:47]
	ds_read_b128 v[68:71], v63 offset:49152
	v_bitop3_b32 v62, v101, v62, 12 bitop3:0x36
	v_lshl_or_b32 v60, v62, 4, v60
	ds_read_b128 v[44:47], v85
	s_waitcnt lgkmcnt(3)
	v_mfma_f32_16x16x32_f16 v[52:55], v[52:55], v[22:25], 0
	ds_read_b128 v[72:75], v60
	ds_read_b128 v[76:79], v84 offset:49152
	v_mad_u32_u24 v105, v103, 3, 2
	v_lshlrev_b32_e32 v133, 4, v105
	s_waitcnt lgkmcnt(4)
	v_mfma_f32_16x16x32_f16 v[52:55], v[56:59], v[18:21], v[52:55]
	ds_read_b128 v[56:59], v85 offset:49152
	v_add_co_u32_e32 v114, vcc, s15, v88
	s_waitcnt lgkmcnt(3)
	v_mfma_f32_16x16x32_f16 v[44:47], v[44:47], v[14:17], v[52:55]
	v_addc_co_u32_e32 v115, vcc, 0, v89, vcc
	v_lshlrev_b32_e32 v31, 2, v31
	s_waitcnt lgkmcnt(2)
	v_mfma_f32_16x16x32_f16 v[44:47], v[72:75], v[10:13], v[44:47]
	ds_read_b128 v[52:55], v60 offset:49152
	v_add_u32_e32 v60, v133, v147
	v_lshlrev_b32_e32 v72, 8, v60
	v_lshlrev_b32_e32 v60, 2, v60
	v_mfma_f32_16x16x32_f16 v[44:47], v[68:71], v[6:9], v[44:47]
	v_and_b32_e32 v60, 12, v60
	v_or_b32_e32 v68, v60, v61
	v_bitop3_b32 v60, v101, v60, v61 bitop3:0x1e
	v_lshl_or_b32 v69, v60, 4, v72
	s_waitcnt lgkmcnt(2)
	v_mfma_f32_16x16x32_f16 v[44:47], v[76:79], v[2:5], v[44:47]
	ds_read_b128 v[60:63], v69
	v_bitop3_b32 v70, v101, v68, 4 bitop3:0x36
	v_lshl_or_b32 v70, v70, 4, v72
	s_waitcnt lgkmcnt(2)
	v_mfma_f32_16x16x32_f16 v[44:47], v[56:59], v[40:43], v[44:47]
	ds_read_b128 v[56:59], v70
	v_bitop3_b32 v71, v101, v68, 8 bitop3:0x36
	v_lshl_or_b32 v71, v71, 4, v72
	s_waitcnt lgkmcnt(1)
	v_mfma_f32_16x16x32_f16 v[22:25], v[60:63], v[22:25], 0
	v_bitop3_b32 v60, v101, v68, 12 bitop3:0x36
	v_lshl_or_b32 v68, v60, 4, v72
	ds_read_b32 v249, v248
	v_mfma_f32_16x16x32_f16 v[126:129], v[52:55], v[106:109], v[44:47]
	s_nop 2
	ds_read_b128 v[44:47], v71
	ds_read_b128 v[52:55], v69 offset:49152
	ds_read_b128 v[60:63], v70 offset:49152
	s_waitcnt lgkmcnt(4)
	v_mfma_f32_16x16x32_f16 v[18:21], v[56:59], v[18:21], v[22:25]
	ds_read_b128 v[56:59], v71 offset:49152
	s_nop 1
	ds_read_b128 v[22:25], v68
	s_waitcnt lgkmcnt(4)
	v_mfma_f32_16x16x32_f16 v[14:17], v[44:47], v[14:17], v[18:21]
	v_add_co_u32_e32 v44, vcc, s5, v88
	s_movk_i32 s5, 0x3000
	s_nop 0
	ds_read_b128 v[18:21], v68 offset:49152
	s_waitcnt lgkmcnt(1)
	v_mfma_f32_16x16x32_f16 v[10:13], v[22:25], v[10:13], v[14:17]
	v_addc_co_u32_e32 v45, vcc, 0, v89, vcc
	v_mfma_f32_16x16x32_f16 v[6:9], v[52:55], v[6:9], v[10:13]
	v_mov_b32_e32 v13, 0xff61b1e6
	v_mfma_f32_16x16x32_f16 v[2:5], v[60:63], v[2:5], v[6:9]
	s_nop 2
	v_add_co_u32_e32 v6, vcc, s5, v88
	v_mfma_f32_16x16x32_f16 v[2:5], v[56:59], v[40:43], v[2:5]
	s_nop 0
	v_addc_co_u32_e32 v7, vcc, 0, v89, vcc
	s_waitcnt lgkmcnt(0)
	v_mfma_f32_16x16x32_f16 v[16:19], v[18:21], v[106:109], v[2:5]
	s_mov_b32 s5, 0xff61b1e6
	s_nop 0
	v_or_b32_e32 v3, s14, v146
	v_mov_b32_e32 v4, 0x7df
	v_med3_u32 v3, v3, 32, v4
	v_or_b32_e32 v4, v97, v102
	v_sub_u32_e32 v3, v4, v3
	v_add_f32_e32 v2, s4, v249
	v_add_u32_e32 v3, 32, v3
	v_mad_u32_u24 v4, v103, 48, v3
	s_movk_i32 s4, 0x41
	v_add_f32_e32 v5, v2, v110
	v_mul_f32_e32 v5, 0x3db8aa3b, v5
	v_cmp_gt_u32_e32 vcc, s4, v4
	v_add_u32_e32 v6, 1, v4
	v_add_f32_e32 v7, v2, v111
	v_cndmask_b32_e32 v5, v13, v5, vcc
	v_mul_f32_e32 v7, 0x3db8aa3b, v7
	v_cmp_gt_u32_e32 vcc, s4, v6
	v_add_u32_e32 v8, 2, v4
	v_add_f32_e32 v9, v2, v112
	v_cndmask_b32_e32 v6, v13, v7, vcc
	v_mul_f32_e32 v9, 0x3db8aa3b, v9
	v_cmp_gt_u32_e32 vcc, s4, v8
	v_add_u32_e32 v4, 3, v4
	v_max3_f32 v7, v5, s5, v6
	v_cndmask_b32_e32 v8, v13, v9, vcc
	v_add_f32_e32 v9, v2, v113
	v_mul_f32_e32 v9, 0x3db8aa3b, v9
	v_cmp_gt_u32_e32 vcc, s4, v4
	v_add_u32_e32 v11, v3, v132
	v_add_f32_e32 v12, v2, v127
	v_cndmask_b32_e32 v10, v13, v9, vcc
	v_max3_f32 v4, v7, v8, v10
	v_add_f32_e32 v7, v2, v126
	v_mul_f32_e32 v7, 0x3db8aa3b, v7
	v_cmp_gt_u32_e32 vcc, s4, v11
	v_add_u32_e32 v9, 1, v11
	v_mul_f32_e32 v12, 0x3db8aa3b, v12
	v_cndmask_b32_e32 v7, v13, v7, vcc
	v_cmp_gt_u32_e32 vcc, s4, v9
	v_add_f32_e32 v14, v2, v128
	v_mul_f32_e32 v14, 0x3db8aa3b, v14
	v_cndmask_b32_e32 v9, v13, v12, vcc
	v_add_u32_e32 v12, 2, v11
	v_cmp_gt_u32_e32 vcc, s4, v12
	v_add_u32_e32 v11, 3, v11
	v_add_u32_e32 v3, v3, v133
	v_cndmask_b32_e32 v12, v13, v14, vcc
	v_add_f32_e32 v14, v2, v129
	v_mul_f32_e32 v14, 0x3db8aa3b, v14
	v_cmp_gt_u32_e32 vcc, s4, v11
	v_add_f32_e32 v11, v2, v16
	v_mul_f32_e32 v11, 0x3db8aa3b, v11
	v_cndmask_b32_e32 v15, v13, v14, vcc
	v_cmp_gt_u32_e32 vcc, s4, v3
	v_add_u32_e32 v14, 1, v3
	v_add_f32_e32 v16, v2, v17
	v_cndmask_b32_e32 v11, v13, v11, vcc
	v_mul_f32_e32 v16, 0x3db8aa3b, v16
	v_cmp_gt_u32_e32 vcc, s4, v14
	v_add_f32_e32 v17, v2, v18
	v_max3_f32 v4, v4, v7, v9
	v_cndmask_b32_e32 v14, v13, v16, vcc
	v_add_u32_e32 v16, 2, v3
	v_mul_f32_e32 v17, 0x3db8aa3b, v17
	v_cmp_gt_u32_e32 vcc, s4, v16
	v_add_u32_e32 v3, 3, v3
	v_add_f32_e32 v2, v2, v19
	v_max3_f32 v4, v4, v12, v15
	v_cndmask_b32_e32 v16, v13, v17, vcc
	v_mul_f32_e32 v2, 0x3db8aa3b, v2
	v_cmp_gt_u32_e32 vcc, s4, v3
	v_max3_f32 v4, v4, v11, v14
	v_lshlrev_b32_e32 v126, 5, v99
	v_cndmask_b32_e32 v17, v13, v2, vcc
	v_max3_f32 v2, v4, v16, v17
	ds_bpermute_b32 v3, v30, v2
	v_lshlrev_b32_e32 v127, 2, v119
	v_lshrrev_b32_e32 v4, 7, v0
	v_cmp_gt_u32_e32 vcc, 16, v98
	s_waitcnt lgkmcnt(0)
	v_max_f32_e32 v3, v3, v3
	v_max_f32_e32 v2, v2, v3
	ds_bpermute_b32 v3, v31, v2
	s_waitcnt lgkmcnt(0)
	v_max_f32_e32 v3, v3, v3
	v_max_f32_e32 v13, v2, v3
	v_and_b32_e32 v2, 0x180, v0
	v_or_b32_e32 v2, 0x23400, v2
	v_lshlrev_b32_e32 v3, 2, v100
	s_and_saveexec_b64 s[4:5], vcc
	v_lshlrev_b32_e32 v18, 6, v103
	v_add3_u32 v18, v2, v18, v3
	ds_write_b32 v18, v13
	s_or_b64 exec, exec, s[4:5]
	v_lshlrev_b32_e32 v18, 4, v103
	v_bitop3_b32 v19, v18, 16, v100 bitop3:0x36
	v_lshl_add_u32 v2, v19, 2, v2
	s_waitcnt lgkmcnt(0)
	s_barrier
	ds_read_b32 v19, v2
	v_max_f32_e32 v13, v13, v13
	v_mul_u32_u24_e32 v20, 0xd00, v4
	s_load_dwordx2 s[0:1], s[0:1], 0x30
	v_or_b32_e32 v2, 1, v124
	s_waitcnt lgkmcnt(0)
	v_max_f32_e32 v19, v19, v19
	v_max_f32_e32 v19, v13, v19
	v_sub_f32_e32 v5, v5, v19
	v_exp_f32_e32 v5, v5
	v_sub_f32_e32 v6, v6, v19
	v_exp_f32_e32 v6, v6
	v_sub_f32_e32 v8, v8, v19
	v_mul_u32_u24_e32 v13, 0xd0, v100
	v_exp_f32_e32 v8, v8
	v_sub_f32_e32 v10, v10, v19
	v_add3_u32 v20, v13, v20, v29
	v_exp_f32_e32 v10, v10
	v_or_b32_e32 v22, 0x20000, v20
	v_add_f32_e32 v20, 0, v5
	v_add_f32_e32 v20, v20, v6
	v_add_f32_e32 v20, v20, v8
	v_add_f32_e32 v23, v20, v10
	v_cvt_pk_f16_f32 v21, v8, v10
	v_cvt_pk_f16_f32 v20, v5, v6
	v_mad_u32_u24 v5, v103, s16, v22
	ds_write_b64 v5, v[20:21]
	v_sub_f32_e32 v5, v7, v19
	v_exp_f32_e32 v5, v5
	v_sub_f32_e32 v6, v9, v19
	v_exp_f32_e32 v6, v6
	v_sub_f32_e32 v7, v12, v19
	v_exp_f32_e32 v7, v7
	v_sub_f32_e32 v8, v15, v19
	v_exp_f32_e32 v8, v8
	v_sub_f32_e32 v10, v11, v19
	v_add_f32_e32 v9, v23, v5
	v_exp_f32_e32 v10, v10
	v_sub_f32_e32 v11, v14, v19
	v_add_f32_e32 v9, v9, v6
	v_exp_f32_e32 v11, v11
	v_sub_f32_e32 v12, v16, v19
	v_add_f32_e32 v9, v9, v7
	v_exp_f32_e32 v12, v12
	v_sub_f32_e32 v14, v17, v19
	v_add_f32_e32 v9, v9, v8
	v_exp_f32_e32 v14, v14
	v_add_f32_e32 v9, v9, v10
	v_add_f32_e32 v9, v9, v11
	v_add_f32_e32 v9, v9, v12
	v_add_f32_e32 v9, v9, v14
	ds_bpermute_b32 v15, v30, v9
	v_cvt_pk_f16_f32 v7, v7, v8
	v_cvt_pk_f16_f32 v6, v5, v6
	v_lshl_add_u32 v5, v104, 5, v22
	ds_write_b64 v5, v[6:7]
	s_waitcnt lgkmcnt(1)
	v_add_f32_e32 v5, v9, v15
	ds_bpermute_b32 v6, v31, v5
	s_movk_i32 s7, 0xd00
	s_mov_b32 s6, 0x20000
	v_cvt_pk_f16_f32 v9, v12, v14
	v_cvt_pk_f16_f32 v8, v10, v11
	v_lshl_add_u32 v7, v105, 5, v22
	ds_write_b64 v7, v[8:9]
	s_and_saveexec_b64 s[4:5], vcc
	s_cbranch_execz .LBB1_4
	v_lshlrev_b32_e32 v4, 5, v4
	v_or_b32_e32 v7, v18, v100
	v_lshlrev_b32_e32 v4, 2, v4
	v_lshlrev_b32_e32 v7, 2, v7
	s_mov_b32 s8, 0x23600
	v_add3_u32 v4, v7, v4, s8
	s_waitcnt lgkmcnt(1)
	v_add_f32_e32 v5, v5, v6
	ds_write_b32 v4, v5
.LBB1_4:
	s_or_b64 exec, exec, s[4:5]
	v_lshl_or_b32 v4, v27, 1, v96
	v_lshl_or_b32 v3, v4, 7, v3
	v_or_b32_e32 v5, 0x23600, v3
	v_or_b32_e32 v3, 0x23640, v3
	s_waitcnt lgkmcnt(0)
	s_barrier
	ds_read_b32 v5, v5
	ds_read_b32 v3, v3
	v_mad_u32_u24 v4, v4, s7, v13
	v_lshl_add_u32 v4, v119, 4, v4
	v_or_b32_e32 v6, 0x20000, v4
	ds_read_b128 v[16:19], v6
	s_waitcnt lgkmcnt(1)
	v_add_f32_e32 v3, v5, v3
	v_add_u32_e32 v5, 0x20020, v4
	v_add_u32_e32 v6, 0x20040, v4
	ds_read_b128 v[112:115], v5
	ds_read_b128 v[108:111], v6
	v_add_u32_e32 v5, 0x20060, v4
	v_add_u32_e32 v6, 0x20080, v4
	v_lshlrev_b32_e32 v7, 1, v101
	ds_read_b128 v[104:107], v5
	ds_read_b128 v[96:99], v6
	v_lshrrev_b32_e32 v5, 2, v100
	v_or_b32_e32 v6, v28, v125
	v_and_b32_e32 v7, 2, v7
	v_bfe_u32 v8, v0, 1, 1
	v_and_b32_e32 v164, 8, v121
	v_bfe_i32 v9, v0, 7, 1
	v_or3_b32 v8, v8, v7, v164
	v_and_b32_e32 v0, 12, v0
	v_add_lshl_u32 v10, v6, v5, 8
	v_or_b32_e32 v5, v6, v5
	v_and_b32_e32 v9, 0xc000, v9
	v_lshlrev_b32_e32 v12, 8, v5
	v_bitop3_b32 v5, v0, v8, v124 bitop3:0x36
	v_lshl_or_b32 v13, v5, 4, v9
	v_bitop3_b32 v6, v0, v8, v2 bitop3:0x36
	v_or_b32_e32 v15, 0x1000, v12
	v_lshl_or_b32 v14, v6, 4, v9
	v_add_u32_e32 v7, v13, v15
	v_or_b32_e32 v24, 0x1400, v12
	v_or_b32_e32 v20, v7, v1
	v_add_u32_e32 v7, v14, v24
	v_add_u32_e32 v25, 0x2000, v10
	v_add_u32_e32 v5, v13, v12
	v_add_u32_e32 v6, v14, v12
	v_or_b32_e32 v22, v7, v1
	v_add_u32_e32 v7, v13, v25
	v_add_u32_e32 v150, 0x3000, v10
	v_or_b32_e32 v8, 4, v8
	v_add_u32_e32 v4, 0x200a0, v4
	v_or_b32_e32 v5, v5, v1
	v_or_b32_e32 v6, v6, v1
	v_or_b32_e32 v27, v7, v1
	v_add_u32_e32 v31, v13, v150
	v_add_u32_e32 v151, 0x3400, v10
	v_bitop3_b32 v124, v0, v8, v124 bitop3:0x36
	v_bitop3_b32 v0, v0, v8, v2 bitop3:0x36
	ds_read_b128 v[100:103], v4
	ds_read_b64_tr_b16 v[4:5], v5
	ds_read_b64_tr_b16 v[6:7], v6 offset:1024
	ds_read_b64_tr_b16 v[20:21], v20
	ds_read_b64_tr_b16 v[22:23], v22
	ds_read_b64_tr_b16 v[28:29], v27
	v_add_u32_e32 v27, 0x2400, v10
	v_or_b32_e32 v128, v31, v1
	v_add_u32_e32 v31, v14, v151
	v_add_u32_e32 v152, 0x4000, v10
	v_add_u32_e32 v158, 0x4400, v10
	v_lshl_or_b32 v124, v124, 4, v9
	v_lshl_or_b32 v0, v0, 4, v9
	v_add_u32_e32 v11, 0x5000, v10
	v_add_u32_e32 v30, v14, v27
	v_or_b32_e32 v130, v31, v1
	v_add_u32_e32 v31, v13, v152
	v_add_u32_e32 v134, v14, v158
	v_add_u32_e32 v10, 0x5400, v10
	v_add_u32_e32 v135, v124, v12
	v_add_u32_e32 v2, v0, v12
	v_add_u32_e32 v8, v124, v15
	v_or_b32_e32 v30, v30, v1
	v_or_b32_e32 v132, v31, v1
	v_or_b32_e32 v134, v134, v1
	v_add_u32_e32 v13, v13, v11
	v_add_u32_e32 v14, v14, v10
	v_or_b32_e32 v140, v135, v1
	v_or_b32_e32 v2, v2, v1
	v_or_b32_e32 v8, v8, v1
	v_add_u32_e32 v9, v0, v24
	v_add_u32_e32 v12, v124, v25
	ds_read_b64_tr_b16 v[30:31], v30
	ds_read_b64_tr_b16 v[128:129], v128
	ds_read_b64_tr_b16 v[130:131], v130
	ds_read_b64_tr_b16 v[132:133], v132
	v_or_b32_e32 v13, v13, v1
	v_or_b32_e32 v14, v14, v1
	ds_read_b64_tr_b16 v[134:135], v134
	ds_read_b64_tr_b16 v[136:137], v13
	ds_read_b64_tr_b16 v[138:139], v14
	ds_read_b64_tr_b16 v[140:141], v140
	v_or_b32_e32 v9, v9, v1
	v_or_b32_e32 v12, v12, v1
	ds_read_b64_tr_b16 v[142:143], v2 offset:1024
	ds_read_b64_tr_b16 v[144:145], v8
	ds_read_b64_tr_b16 v[146:147], v9
	ds_read_b64_tr_b16 v[148:149], v12
	v_add_u32_e32 v2, v0, v27
	v_add_u32_e32 v8, v124, v150
	v_or_b32_e32 v2, v2, v1
	v_or_b32_e32 v8, v8, v1
	v_add_u32_e32 v9, v0, v151
	v_add_u32_e32 v12, v124, v152
	v_or_b32_e32 v9, v9, v1
	v_or_b32_e32 v12, v12, v1
	ds_read_b64_tr_b16 v[150:151], v2
	ds_read_b64_tr_b16 v[152:153], v8
	ds_read_b64_tr_b16 v[154:155], v9
	ds_read_b64_tr_b16 v[156:157], v12
	v_add_u32_e32 v2, v0, v158
	v_add_u32_e32 v8, v124, v11
	v_add_u32_e32 v0, v0, v10
	v_or_b32_e32 v2, v2, v1
	v_or_b32_e32 v8, v8, v1
	v_or_b32_e32 v0, v0, v1
	v_div_scale_f32 v1, s[8:9], v3, v3, 1.0
	v_rcp_f32_e32 v9, v1
	ds_read_b64_tr_b16 v[158:159], v2
	ds_read_b64_tr_b16 v[160:161], v8
	ds_read_b64_tr_b16 v[162:163], v0
	s_mov_b32 s4, 0xc000
	s_movk_i32 s5, 0x4000
	v_fma_f32 v0, -v1, v9, 1.0
	v_fmac_f32_e32 v9, v0, v9
	v_div_scale_f32 v0, vcc, 1.0, v3, 1.0
	v_mul_f32_e32 v2, v0, v9
	v_fma_f32 v8, -v1, v2, v0
	v_fmac_f32_e32 v2, v8, v9
	v_fma_f32 v0, -v1, v2, v0
	v_div_fmas_f32 v0, v0, v9, v2
	v_div_fixup_f32 v124, v0, v3, 1.0
	s_waitcnt lgkmcnt(14)
	v_mfma_f32_32x32x16_f16 v[0:15], v[4:7], v[16:19], 0
	s_mov_b32 s7, 0x18000
	v_lshlrev_b32_e32 v172, 2, v126
	v_mov_b32_e32 v173, 0
	v_mfma_f32_32x32x16_f16 v[0:15], v[20:23], v[112:115], v[0:15]
	v_or_b32_e32 v20, v26, v116
	v_and_b32_e32 v21, 0x4000, v118
	v_lshl_or_b32 v20, v20, 8, v21
	v_bitop3_b32 v118, v121, v120, 8 bitop3:0x6c
	v_or3_b32 v121, v20, v125, s7
	v_mfma_f32_32x32x16_f16 v[0:15], v[28:31], v[108:111], v[0:15]
	v_mfma_f32_32x32x16_f16 v[0:15], v[128:131], v[104:107], v[0:15]
	v_mfma_f32_32x32x16_f16 v[0:15], v[132:135], v[96:99], v[0:15]
	s_waitcnt lgkmcnt(12)
	v_mfma_f32_32x32x16_f16 v[0:15], v[136:139], v[100:103], v[0:15]
	s_nop 11
	v_fma_mixlo_f16 v20, v124, v0, 0
	v_mov_b32_e32 v0, v1
	v_mov_b32_e32 v1, v2
	v_pk_mul_f32 v[0:1], v[124:125], v[0:1] op_sel_hi:[0,1]
	v_cvt_pk_f16_f32 v1, v0, v1
	v_pack_b32_f16 v0, v20, v1
	s_waitcnt lgkmcnt(10)
	v_mfma_f32_32x32x16_f16 v[16:31], v[140:143], v[16:19], 0
	v_fma_mixlo_f16 v2, v124, v3, 0
	v_alignbit_b32 v1, v2, v1, 16
	v_lshl_or_b32 v2, v118, 4, v121
	ds_write_b64 v2, v[0:1]
	v_mov_b32_e32 v0, v5
	v_mov_b32_e32 v1, v6
	v_pk_mul_f32 v[0:1], v[124:125], v[0:1] op_sel_hi:[0,1]
	s_waitcnt lgkmcnt(9)
	v_mfma_f32_32x32x16_f16 v[16:31], v[144:147], v[112:115], v[16:31]
	v_fma_mixlo_f16 v2, v124, v4, 0
	v_cvt_pk_f16_f32 v1, v0, v1
	v_pack_b32_f16 v0, v2, v1
	v_fma_mixlo_f16 v2, v124, v7, 0
	v_alignbit_b32 v1, v2, v1, 16
	v_bitop3_b32 v2, v164, v120, 1 bitop3:0x36
	v_lshl_or_b32 v2, v2, 4, v121
	s_waitcnt lgkmcnt(7)
	v_mfma_f32_32x32x16_f16 v[16:31], v[148:151], v[108:111], v[16:31]
	ds_write_b64 v2, v[0:1]
	v_mov_b32_e32 v0, v9
	v_mov_b32_e32 v1, v10
	v_mul_f32_e64 v0, v124, v0
	v_mul_f32_e64 v1, v124, v1
	v_fma_mixlo_f16 v2, v124, v8, 0
	v_cvt_pk_f16_f32 v1, v0, v1
	v_pack_b32_f16 v0, v2, v1
	s_waitcnt lgkmcnt(6)
	v_mfma_f32_32x32x16_f16 v[16:31], v[152:155], v[104:107], v[16:31]
	v_fma_mixlo_f16 v2, v124, v11, 0
	v_alignbit_b32 v1, v2, v1, 16
	v_bitop3_b32 v2, v164, v120, 2 bitop3:0x36
	v_lshl_or_b32 v2, v2, 4, v121
	ds_write_b64 v2, v[0:1]
	v_mov_b32_e32 v0, v13
	v_mov_b32_e32 v1, v14
	s_waitcnt lgkmcnt(5)
	v_mfma_f32_32x32x16_f16 v[16:31], v[156:159], v[96:99], v[16:31]
	v_mul_f32_e64 v0, v124, v0
	v_mul_f32_e64 v1, v124, v1
	v_fma_mixlo_f16 v2, v124, v12, 0
	v_cvt_pk_f16_f32 v1, v0, v1
	v_pack_b32_f16 v0, v2, v1
	v_fma_mixlo_f16 v2, v124, v15, 0
	v_alignbit_b32 v1, v2, v1, 16
	v_bitop3_b32 v2, v164, v120, 3 bitop3:0x36
	s_waitcnt lgkmcnt(3)
	v_mfma_f32_32x32x16_f16 v[16:31], v[160:163], v[100:103], v[16:31]
	v_lshl_or_b32 v2, v2, 4, v121
	ds_write_b64 v2, v[0:1]
	s_nop 9
	v_mov_b32_e32 v0, v17
	v_mov_b32_e32 v1, v18
	v_pk_mul_f32 v[0:1], v[124:125], v[0:1] op_sel_hi:[0,1]
	v_fma_mixlo_f16 v2, v124, v16, 0
	v_cvt_pk_f16_f32 v1, v0, v1
	v_pack_b32_f16 v0, v2, v1
	v_fma_mixlo_f16 v2, v124, v19, 0
	v_alignbit_b32 v1, v2, v1, 16
	v_bitop3_b32 v2, v164, v120, 4 bitop3:0x36
	v_lshl_or_b32 v2, v2, 4, v121
	ds_write_b64 v2, v[0:1]
	v_mov_b32_e32 v0, v21
	v_mov_b32_e32 v1, v22
	v_pk_mul_f32 v[0:1], v[124:125], v[0:1] op_sel_hi:[0,1]
	v_fma_mixlo_f16 v2, v124, v20, 0
	v_cvt_pk_f16_f32 v1, v0, v1
	v_pack_b32_f16 v0, v2, v1
	v_fma_mixlo_f16 v2, v124, v23, 0
	v_alignbit_b32 v1, v2, v1, 16
	v_bitop3_b32 v2, v164, v120, 5 bitop3:0x36
	v_lshl_or_b32 v2, v2, 4, v121
	ds_write_b64 v2, v[0:1]
	v_mov_b32_e32 v0, v25
	v_mov_b32_e32 v1, v26
	v_pk_mul_f32 v[0:1], v[124:125], v[0:1] op_sel_hi:[0,1]
	v_fma_mixlo_f16 v2, v124, v24, 0
	v_cvt_pk_f16_f32 v1, v0, v1
	v_pack_b32_f16 v0, v2, v1
	v_fma_mixlo_f16 v2, v124, v27, 0
	v_alignbit_b32 v1, v2, v1, 16
	v_bitop3_b32 v2, v164, v120, 6 bitop3:0x36
	v_lshl_or_b32 v2, v2, 4, v121
	ds_write_b64 v2, v[0:1]
	v_mov_b32_e32 v0, v29
	v_mov_b32_e32 v1, v30
	v_pk_mul_f32 v[0:1], v[124:125], v[0:1] op_sel_hi:[0,1]
	v_fma_mixlo_f16 v2, v124, v28, 0
	v_cvt_pk_f16_f32 v1, v0, v1
	v_pack_b32_f16 v0, v2, v1
	v_fma_mixlo_f16 v2, v124, v31, 0
	v_alignbit_b32 v1, v2, v1, 16
	v_bitop3_b32 v2, v164, v120, 7 bitop3:0x36
	v_lshl_or_b32 v2, v2, 4, v121
	ds_write_b64 v2, v[0:1]
	v_lshl_add_u64 v[0:1], s[0:1], 0, v[172:173]
	v_lshlrev_b32_e32 v172, 2, v127
	v_lshl_add_u64 v[0:1], v[0:1], 0, v[172:173]
	s_waitcnt lgkmcnt(0)
	s_barrier
	global_load_dwordx4 v[108:111], v[0:1], off
	global_load_dwordx4 v[104:107], v[0:1], off offset:32
	global_load_dwordx4 v[100:103], v[0:1], off offset:64
	global_load_dwordx4 v[96:99], v[0:1], off offset:96
	v_xor_b32_e32 v0, v119, v120
	v_bitop3_b32 v8, v119, v120, 2 bitop3:0x36
	v_lshlrev_b32_e32 v172, 4, v0
	v_lshlrev_b32_e32 v174, 4, v8
	v_add_u32_e32 v0, v117, v172
	v_add_u32_e32 v8, v117, v174
	v_or_b32_e32 v1, 0x18000, v0
	v_add_u32_e32 v4, 0x1a000, v0
	v_or_b32_e32 v9, 0x18000, v8
	v_add_u32_e32 v8, 0x1a000, v8
	ds_read_b128 v[0:3], v1
	ds_read_b128 v[4:7], v4
	ds_read_b128 v[112:115], v9
	ds_read_b128 v[128:131], v8
	v_bitop3_b32 v8, v119, v120, 4 bitop3:0x36
	v_lshlrev_b32_e32 v175, 4, v8
	v_add_u32_e32 v8, v117, v175
	v_or_b32_e32 v9, 0x18000, v8
	v_add_u32_e32 v8, 0x1a000, v8
	ds_read_b128 v[132:135], v9
	ds_read_b128 v[136:139], v8
	v_bitop3_b32 v8, v119, v120, 6 bitop3:0x36
	v_lshlrev_b32_e32 v176, 4, v8
	v_add_u32_e32 v8, v117, v176
	v_or_b32_e32 v9, 0x18000, v8
	v_add_u32_e32 v8, 0x1a000, v8
	ds_read_b128 v[140:143], v9
	ds_read_b128 v[144:147], v8
	v_bitop3_b32 v8, v119, v120, 8 bitop3:0x36
	v_lshlrev_b32_e32 v177, 4, v8
	v_add_u32_e32 v8, v122, v177
	v_add_u32_e32 v9, v123, v177
	ds_read_b128 v[148:151], v8
	ds_read_b128 v[152:155], v9
	v_bitop3_b32 v8, v119, v120, 10 bitop3:0x36
	v_lshlrev_b32_e32 v178, 4, v8
	v_add_u32_e32 v8, v122, v178
	v_add_u32_e32 v9, v123, v178
	ds_read_b128 v[156:159], v8
	ds_read_b128 v[160:163], v9
	v_bitop3_b32 v8, v119, v120, 12 bitop3:0x36
	v_lshlrev_b32_e32 v179, 4, v8
	v_add_u32_e32 v8, v122, v179
	v_add_u32_e32 v9, v123, v179
	ds_read_b128 v[164:167], v8
	ds_read_b128 v[168:171], v9
	v_bitop3_b32 v8, v119, v120, 14 bitop3:0x36
	v_lshlrev_b32_e32 v180, 4, v8
	v_add_u32_e32 v8, v122, v180
	v_add_u32_e32 v9, v123, v180
	ds_read_b128 v[118:121], v8
	ds_read_b128 v[122:125], v9
	s_waitcnt vmcnt(19) lgkmcnt(14)
	v_mfma_f32_32x32x16_f16 v[16:31], v[184:187], v[0:3], 0
	v_mfma_f32_32x32x16_f16 v[0:15], v[184:187], v[4:7], 0
	s_waitcnt vmcnt(18) lgkmcnt(13)
	v_mfma_f32_32x32x16_f16 v[16:31], v[188:191], v[112:115], v[16:31]
	s_waitcnt lgkmcnt(12)
	v_mfma_f32_32x32x16_f16 v[0:15], v[188:191], v[128:131], v[0:15]
	s_waitcnt vmcnt(17) lgkmcnt(11)
	v_mfma_f32_32x32x16_f16 v[16:31], v[192:195], v[132:135], v[16:31]
	s_waitcnt lgkmcnt(10)
	v_mfma_f32_32x32x16_f16 v[0:15], v[192:195], v[136:139], v[0:15]
	s_waitcnt vmcnt(16) lgkmcnt(9)
	v_mfma_f32_32x32x16_f16 v[16:31], v[196:199], v[140:143], v[16:31]
	s_waitcnt lgkmcnt(8)
	v_mfma_f32_32x32x16_f16 v[0:15], v[196:199], v[144:147], v[0:15]
	v_or_b32_e32 v140, 0x1c000, v117
	v_or_b32_e32 v117, 0x1e000, v117
	v_add_u32_e32 v32, v140, v172
	v_add_u32_e32 v36, v117, v172
	v_add_u32_e32 v48, v140, v174
	v_add_u32_e32 v64, v117, v174
	v_add_u32_e32 v112, v140, v175
	v_add_u32_e32 v128, v117, v175
	v_add_u32_e32 v132, v140, v176
	v_add_u32_e32 v136, v117, v176
	ds_read_b128 v[32:35], v32
	ds_read_b128 v[36:39], v36
	ds_read_b128 v[48:51], v48
	ds_read_b128 v[64:67], v64
	ds_read_b128 v[112:115], v112
	ds_read_b128 v[128:131], v128
	ds_read_b128 v[132:135], v132
	ds_read_b128 v[136:139], v136
	s_waitcnt vmcnt(13) lgkmcnt(14)
	v_mfma_f32_32x32x16_f16 v[16:31], v[200:203], v[148:151], v[16:31]
	v_mfma_f32_32x32x16_f16 v[0:15], v[200:203], v[152:155], v[0:15]
	s_waitcnt lgkmcnt(13)
	v_mfma_f32_32x32x16_f16 v[16:31], v[204:207], v[156:159], v[16:31]
	s_waitcnt lgkmcnt(12)
	v_mfma_f32_32x32x16_f16 v[0:15], v[204:207], v[160:163], v[0:15]
	s_waitcnt lgkmcnt(11)
	v_mfma_f32_32x32x16_f16 v[16:31], v[208:211], v[164:167], v[16:31]
	s_waitcnt lgkmcnt(10)
	v_mfma_f32_32x32x16_f16 v[0:15], v[208:211], v[168:171], v[0:15]
	s_waitcnt vmcnt(8) lgkmcnt(9)
	v_mfma_f32_32x32x16_f16 v[16:31], v[212:215], v[118:121], v[16:31]
	s_waitcnt lgkmcnt(8)
	v_mfma_f32_32x32x16_f16 v[0:15], v[212:215], v[122:125], v[0:15]
	v_add_u32_e32 v80, v140, v177
	v_add_u32_e32 v84, v117, v177
	v_add_u32_e32 v88, v140, v178
	v_add_u32_e32 v92, v117, v178
	v_add_u32_e32 v118, v140, v179
	v_add_u32_e32 v122, v117, v179
	v_add_u32_e32 v140, v140, v180
	ds_read_b128 v[80:83], v80
	ds_read_b128 v[84:87], v84
	ds_read_b128 v[88:91], v88
	ds_read_b128 v[92:95], v92
	ds_read_b128 v[118:121], v118
	ds_read_b128 v[122:125], v122
	v_add_u32_e32 v117, v117, v180
	ds_read_b128 v[140:143], v140
	ds_read_b128 v[144:147], v117
	s_waitcnt lgkmcnt(14)
	v_mfma_f32_32x32x16_f16 v[16:31], v[216:219], v[32:35], v[16:31]
	v_mfma_f32_32x32x16_f16 v[0:15], v[216:219], v[36:39], v[0:15]
	s_waitcnt lgkmcnt(13)
	v_mfma_f32_32x32x16_f16 v[16:31], v[220:223], v[48:51], v[16:31]
	s_waitcnt lgkmcnt(12)
	v_mfma_f32_32x32x16_f16 v[0:15], v[220:223], v[64:67], v[0:15]
	s_waitcnt lgkmcnt(11)
	v_mfma_f32_32x32x16_f16 v[16:31], v[224:227], v[112:115], v[16:31]
	s_waitcnt lgkmcnt(10)
	v_mfma_f32_32x32x16_f16 v[0:15], v[224:227], v[128:131], v[0:15]
	s_waitcnt lgkmcnt(9)
	v_mfma_f32_32x32x16_f16 v[16:31], v[228:231], v[132:135], v[16:31]
	s_waitcnt lgkmcnt(8)
	v_mfma_f32_32x32x16_f16 v[0:15], v[228:231], v[136:139], v[0:15]
	s_waitcnt vmcnt(7) lgkmcnt(7)
	v_mfma_f32_32x32x16_f16 v[16:31], v[232:235], v[80:83], v[16:31]
	s_waitcnt lgkmcnt(6)
	v_mfma_f32_32x32x16_f16 v[0:15], v[232:235], v[84:87], v[0:15]
	s_waitcnt vmcnt(6) lgkmcnt(5)
	v_mfma_f32_32x32x16_f16 v[16:31], v[236:239], v[88:91], v[16:31]
	s_waitcnt lgkmcnt(4)
	v_mfma_f32_32x32x16_f16 v[0:15], v[236:239], v[92:95], v[0:15]
	s_waitcnt vmcnt(5) lgkmcnt(3)
	v_mfma_f32_32x32x16_f16 v[16:31], v[240:243], v[118:121], v[16:31]
	s_waitcnt lgkmcnt(2)
	v_mfma_f32_32x32x16_f16 v[0:15], v[240:243], v[122:125], v[0:15]
	s_waitcnt vmcnt(4) lgkmcnt(1)
	v_mfma_f32_32x32x16_f16 v[16:31], v[244:247], v[140:143], v[16:31]
	s_waitcnt lgkmcnt(0)
	v_mfma_f32_32x32x16_f16 v[0:15], v[244:247], v[144:147], v[0:15]
	s_lshl_b64 s[0:1], s[2:3], 22
	s_add_u32 s0, s12, s0
	v_or_b32_e32 v32, s14, v116
	s_addc_u32 s1, s13, s1
	v_lshlrev_b32_e32 v172, 3, v32
	v_or_b32_e32 v36, v126, v127
	v_lshl_add_u64 v[32:33], s[0:1], 0, v[172:173]
	v_lshlrev_b32_e32 v172, 14, v36
	v_lshl_add_u64 v[32:33], v[32:33], 0, v[172:173]
	s_nop 0
	v_mov_b32_e32 v34, v16
	s_nop 0
	v_mov_b32_e32 v35, v0
	v_mov_b32_e32 v0, v17
	v_add_co_u32_e32 v16, vcc, s5, v32
	s_waitcnt vmcnt(3)
	v_pk_add_f32 v[0:1], v[108:109], v[0:1] op_sel:[1,0]
	v_addc_co_u32_e32 v17, vcc, 0, v33, vcc
	s_mov_b32 s0, 0x8000
	global_store_dwordx2 v[16:17], v[0:1], off nt
	v_mov_b32_e32 v0, v18
	v_mov_b32_e32 v1, v2
	v_add_co_u32_e32 v16, vcc, s0, v32
	v_pk_add_f32 v[0:1], v[110:111], v[0:1] op_sel_hi:[0,1]
	s_nop 0
	v_addc_co_u32_e32 v17, vcc, 0, v33, vcc
	global_store_dwordx2 v[16:17], v[0:1], off nt
	v_mov_b32_e32 v0, v111
	v_mov_b32_e32 v2, v19
	v_pk_add_f32 v[0:1], v[0:1], v[2:3] op_sel_hi:[0,1]
	v_add_co_u32_e32 v2, vcc, s4, v32
	s_mov_b32 s0, 0x24000
	s_nop 0
	v_addc_co_u32_e32 v3, vcc, 0, v33, vcc
	global_store_dwordx2 v[2:3], v[0:1], off nt
	v_mov_b32_e32 v0, v20
	v_mov_b32_e32 v1, v4
	v_add_co_u32_e32 v2, vcc, s6, v32
	s_waitcnt vmcnt(5)
	v_pk_add_f32 v[0:1], v[104:105], v[0:1] op_sel_hi:[0,1]
	v_addc_co_u32_e32 v3, vcc, 0, v33, vcc
	global_store_dwordx2 v[2:3], v[0:1], off nt
	v_mov_b32_e32 v4, v21
	v_add_co_u32_e32 v2, vcc, s0, v32
	v_pk_add_f32 v[0:1], v[104:105], v[4:5] op_sel:[1,0]
	s_nop 0
	v_addc_co_u32_e32 v3, vcc, 0, v33, vcc
	s_mov_b32 s0, 0x28000
	global_store_dwordx2 v[2:3], v[0:1], off nt
	v_mov_b32_e32 v0, v22
	v_mov_b32_e32 v1, v6
	v_add_co_u32_e32 v2, vcc, s0, v32
	v_pk_add_f32 v[0:1], v[106:107], v[0:1] op_sel_hi:[0,1]
	s_nop 0
	v_addc_co_u32_e32 v3, vcc, 0, v33, vcc
	s_mov_b32 s0, 0x2c000
	global_store_dwordx2 v[2:3], v[0:1], off nt
	v_mov_b32_e32 v0, v107
	v_mov_b32_e32 v6, v23
	v_add_co_u32_e32 v2, vcc, s0, v32
	v_pk_add_f32 v[0:1], v[0:1], v[6:7] op_sel_hi:[0,1]
	s_nop 0
	v_addc_co_u32_e32 v3, vcc, 0, v33, vcc
	s_mov_b32 s0, 0x40000
	global_store_dwordx2 v[2:3], v[0:1], off nt
	v_mov_b32_e32 v0, v24
	v_mov_b32_e32 v1, v8
	v_add_co_u32_e32 v2, vcc, s0, v32
	s_waitcnt vmcnt(8)
	v_pk_add_f32 v[0:1], v[100:101], v[0:1] op_sel_hi:[0,1]
	v_addc_co_u32_e32 v3, vcc, 0, v33, vcc
	s_mov_b32 s0, 0x44000
	global_store_dwordx2 v[2:3], v[0:1], off nt
	v_mov_b32_e32 v8, v25
	v_add_co_u32_e32 v2, vcc, s0, v32
	v_pk_add_f32 v[0:1], v[100:101], v[8:9] op_sel:[1,0]
	s_nop 0
	v_addc_co_u32_e32 v3, vcc, 0, v33, vcc
	s_mov_b32 s0, 0x48000
	global_store_dwordx2 v[2:3], v[0:1], off nt
	v_mov_b32_e32 v0, v26
	v_mov_b32_e32 v1, v10
	v_add_co_u32_e32 v2, vcc, s0, v32
	v_pk_add_f32 v[0:1], v[102:103], v[0:1] op_sel_hi:[0,1]
	s_nop 0
	v_addc_co_u32_e32 v3, vcc, 0, v33, vcc
	s_mov_b32 s0, 0x4c000
	global_store_dwordx2 v[2:3], v[0:1], off nt
	v_mov_b32_e32 v0, v103
	v_mov_b32_e32 v10, v27
	v_add_co_u32_e32 v2, vcc, s0, v32
	v_pk_add_f32 v[0:1], v[0:1], v[10:11] op_sel_hi:[0,1]
	s_nop 0
	v_addc_co_u32_e32 v3, vcc, 0, v33, vcc
	s_mov_b32 s0, 0x60000
	global_store_dwordx2 v[2:3], v[0:1], off nt
	v_mov_b32_e32 v0, v28
	v_mov_b32_e32 v1, v12
	v_add_co_u32_e32 v2, vcc, s0, v32
	s_waitcnt vmcnt(11)
	v_pk_add_f32 v[0:1], v[96:97], v[0:1] op_sel_hi:[0,1]
	v_addc_co_u32_e32 v3, vcc, 0, v33, vcc
	s_mov_b32 s0, 0x64000
	global_store_dwordx2 v[2:3], v[0:1], off nt
	v_mov_b32_e32 v12, v29
	v_add_co_u32_e32 v2, vcc, s0, v32
	v_pk_add_f32 v[0:1], v[96:97], v[12:13] op_sel:[1,0]
	s_nop 0
	v_addc_co_u32_e32 v3, vcc, 0, v33, vcc
	s_mov_b32 s0, 0x68000
	global_store_dwordx2 v[2:3], v[0:1], off nt
	v_mov_b32_e32 v0, v30
	v_mov_b32_e32 v1, v14
	v_add_co_u32_e32 v2, vcc, s0, v32
	v_pk_add_f32 v[0:1], v[98:99], v[0:1] op_sel_hi:[0,1]
	s_nop 0
	v_addc_co_u32_e32 v3, vcc, 0, v33, vcc
	global_store_dwordx2 v[2:3], v[0:1], off nt
	v_mov_b32_e32 v0, v99
	v_mov_b32_e32 v14, v31
	v_add_co_u32_e32 v2, vcc, 0x6c000, v32
	v_pk_add_f32 v[34:35], v[108:109], v[34:35] op_sel_hi:[0,1]
	v_pk_add_f32 v[0:1], v[0:1], v[14:15] op_sel_hi:[0,1]
	v_addc_co_u32_e32 v3, vcc, 0, v33, vcc
	global_store_dwordx2 v[32:33], v[34:35], off nt
	global_store_dwordx2 v[2:3], v[0:1], off nt
	s_endpgm

	.amdhsa_kernel _Z7na_mainPKDF16_PKhS0_PKfS4_S4_S4_Pf
		.amdhsa_group_segment_fixed_size 162048
		.amdhsa_private_segment_fixed_size 0
		.amdhsa_kernarg_size 64
		.amdhsa_user_sgpr_count 2
		.amdhsa_user_sgpr_dispatch_ptr 0
		.amdhsa_user_sgpr_queue_ptr 0
		.amdhsa_user_sgpr_kernarg_segment_ptr 1
		.amdhsa_user_sgpr_dispatch_id 0
		.amdhsa_user_sgpr_kernarg_preload_length 0
		.amdhsa_user_sgpr_kernarg_preload_offset 0
		.amdhsa_user_sgpr_private_segment_size 0
		.amdhsa_uses_dynamic_stack 0
		.amdhsa_enable_private_segment 0
		.amdhsa_system_sgpr_workgroup_id_x 1
		.amdhsa_system_sgpr_workgroup_id_y 0
		.amdhsa_system_sgpr_workgroup_id_z 0
		.amdhsa_system_sgpr_workgroup_info 0
		.amdhsa_system_vgpr_workitem_id 0
		.amdhsa_next_free_vgpr 254
		.amdhsa_next_free_sgpr 96
		.amdhsa_accum_offset 256
		.amdhsa_reserve_vcc 1
		.amdhsa_float_round_mode_32 0
		.amdhsa_float_round_mode_16_64 0
		.amdhsa_float_denorm_mode_32 3
		.amdhsa_float_denorm_mode_16_64 3
		.amdhsa_dx10_clamp 1
		.amdhsa_ieee_mode 1
		.amdhsa_fp16_overflow 0
		.amdhsa_tg_split 0
		.amdhsa_exception_fp_ieee_invalid_op 0
		.amdhsa_exception_fp_denorm_src 0
		.amdhsa_exception_fp_ieee_div_zero 0
		.amdhsa_exception_fp_ieee_overflow 0
		.amdhsa_exception_fp_ieee_underflow 0
		.amdhsa_exception_fp_ieee_inexact 0
		.amdhsa_exception_int_div_zero 0
	.end_amdhsa_kernel

amdhsa.kernels:
  - .agpr_count:     16
    .args:
      - .actual_access:  read_only
        .address_space:  global
        .offset:         0
        .size:           8
        .value_kind:     global_buffer
      - .actual_access:  read_only
        .address_space:  global
        .offset:         8
        .size:           8
        .value_kind:     global_buffer
      - .actual_access:  read_only
        .address_space:  global
        .offset:         16
        .size:           8
        .value_kind:     global_buffer
      - .actual_access:  read_only
        .address_space:  global
        .offset:         24
        .size:           8
        .value_kind:     global_buffer
      - .actual_access:  read_only
        .address_space:  global
        .offset:         32
        .size:           8
        .value_kind:     global_buffer
      - .actual_access:  read_only
        .address_space:  global
        .offset:         40
        .size:           8
        .value_kind:     global_buffer
      - .actual_access:  write_only
        .address_space:  global
        .offset:         48
        .size:           8
        .value_kind:     global_buffer
      - .actual_access:  write_only
        .address_space:  global
        .offset:         56
        .size:           8
        .value_kind:     global_buffer
      - .actual_access:  write_only
        .address_space:  global
        .offset:         64
        .size:           8
        .value_kind:     global_buffer
      - .actual_access:  write_only
        .address_space:  global
        .offset:         72
        .size:           8
        .value_kind:     global_buffer
      - .actual_access:  write_only
        .address_space:  global
        .offset:         80
        .size:           8
        .value_kind:     global_buffer
      - .actual_access:  write_only
        .address_space:  global
        .offset:         88
        .size:           8
        .value_kind:     global_buffer
    .group_segment_fixed_size: 16384
    .kernarg_segment_align: 8
    .kernarg_segment_size: 96
    .language:       OpenCL C
    .language_version:
      - 2
      - 0
    .max_flat_workgroup_size: 256
    .name:           _Z7na_prepPKfS0_S0_S0_S0_S0_PDF16_PhS1_PfS3_S3_
    .private_segment_fixed_size: 0
    .sgpr_count:     23
    .sgpr_spill_count: 0
    .symbol:         _Z7na_prepPKfS0_S0_S0_S0_S0_PDF16_PhS1_PfS3_S3_.kd
    .uniform_work_group_size: 1
    .uses_dynamic_stack: false
    .vgpr_count:     116
    .vgpr_spill_count: 0
    .wavefront_size: 64
  - .agpr_count:     0
    .args:
      - .address_space:  global
        .offset:         0
        .size:           8
        .value_kind:     global_buffer
      - .actual_access:  read_only
        .address_space:  global
        .offset:         8
        .size:           8
        .value_kind:     global_buffer
      - .actual_access:  read_only
        .address_space:  global
        .offset:         16
        .size:           8
        .value_kind:     global_buffer
      - .actual_access:  read_only
        .address_space:  global
        .offset:         24
        .size:           8
        .value_kind:     global_buffer
      - .actual_access:  read_only
        .address_space:  global
        .offset:         32
        .size:           8
        .value_kind:     global_buffer
      - .actual_access:  read_only
        .address_space:  global
        .offset:         40
        .size:           8
        .value_kind:     global_buffer
      - .actual_access:  read_only
        .address_space:  global
        .offset:         48
        .size:           8
        .value_kind:     global_buffer
      - .actual_access:  write_only
        .address_space:  global
        .offset:         56
        .size:           8
        .value_kind:     global_buffer
    .group_segment_fixed_size: 162048
    .kernarg_segment_align: 8
    .kernarg_segment_size: 64
    .language:       OpenCL C
    .language_version:
      - 2
      - 0
    .max_flat_workgroup_size: 512
    .name:           _Z7na_mainPKDF16_PKhS0_PKfS4_S4_S4_Pf
    .private_segment_fixed_size: 0
    .sgpr_count:     24
    .sgpr_spill_count: 0
    .symbol:         _Z7na_mainPKDF16_PKhS0_PKfS4_S4_S4_Pf.kd
    .uniform_work_group_size: 1
    .uses_dynamic_stack: false
    .vgpr_count:     254
    .vgpr_spill_count: 0
    .wavefront_size: 64
